# MoE gather phase: the eight per-expert count loads of a CNT row become one 32-byte load (was eight serial round trips)
# speedup vs baseline: 1.0176x; 1.0006x over previous
; __global__ void __launch_bounds__(NWAVES * 64, 2) trunk_fwd(Args args) {
;     ...
;             for (int base = 0; base < G; base += 512) {
;                 const int bb = base + tid;
; #pragma unroll
;                 for (int e = 0; e < 8; ++e) { const int c = bb < G ? CNT[bb * 32 + e] : 0; const float tot = wave_sum((float)c), bef = wave_sum(bb < bx ? (float)c : 0.f);
;                     if (lane == 0) { atomicAdd((int*)&SH[e], (int)tot); atomicAdd((int*)&SH[8 + e], (int)bef); } } }
.LBB0_837:
	s_waitcnt lgkmcnt(1)
	v_add_u32_e32 v12, s16, v2
	v_lshlrev_b32_e32 v4, 5, v12
	v_cmp_gt_i32_e64 s[6:7], s33, v12
	v_mov_b32_e32 v11, 0
	s_waitcnt lgkmcnt(0)
	v_ashrrev_i32_e32 v5, 31, v4
	s_and_saveexec_b64 s[4:5], s[6:7]
	s_cbranch_execz .LBB0_839
	v_readlane_b32 s8, v252, 18
	v_readlane_b32 s9, v252, 19
	s_nop 1
	v_lshl_add_u64 v[14:15], v[4:5], 2, s[8:9]
	global_load_dwordx4 v[232:235], v[14:15], off
	global_load_dwordx4 v[236:239], v[14:15], off offset:16
	s_waitcnt vmcnt(0)
	v_cvt_f32_i32_e32 v11, v232

; __global__ void __launch_bounds__(NWAVES * 64, 2) trunk_fwd(Args args) {
;     ...
;                 for (int e = 0; e < 8; ++e) { const int c = bb < G ? CNT[bb * 32 + e] : 0; const float tot = wave_sum((float)c), bef = wave_sum(bb < bx ? (float)c : 0.f);
;                     if (lane == 0) { atomicAdd((int*)&SH[e], (int)tot); atomicAdd((int*)&SH[8 + e], (int)bef); } } }
.LBB0_848:
	s_or_b64 exec, exec, s[12:13]
	v_mov_b32_e32 v11, 0
	s_and_saveexec_b64 s[8:9], s[6:7]
	s_cbranch_execz .LBB0_850
	v_readlane_b32 s12, v252, 18
	v_readlane_b32 s13, v252, 19
	s_waitcnt lgkmcnt(0)
	s_nop 0
	v_lshl_add_u64 v[12:13], v[4:5], 2, s[12:13]
	v_cvt_f32_i32_e32 v11, v233

; __global__ void __launch_bounds__(NWAVES * 64, 2) trunk_fwd(Args args) {
;     ...
;                 for (int e = 0; e < 8; ++e) { const int c = bb < G ? CNT[bb * 32 + e] : 0; const float tot = wave_sum((float)c), bef = wave_sum(bb < bx ? (float)c : 0.f);
;                     if (lane == 0) { atomicAdd((int*)&SH[e], (int)tot); atomicAdd((int*)&SH[8 + e], (int)bef); } } }
.LBB0_859:
	s_or_b64 exec, exec, s[12:13]
	v_mov_b32_e32 v11, 0
	s_and_saveexec_b64 s[8:9], s[6:7]
	s_cbranch_execz .LBB0_861
	v_readlane_b32 s12, v252, 18
	v_readlane_b32 s13, v252, 19
	s_waitcnt lgkmcnt(0)
	s_nop 0
	v_lshl_add_u64 v[12:13], v[4:5], 2, s[12:13]
	v_cvt_f32_i32_e32 v11, v234

; __global__ void __launch_bounds__(NWAVES * 64, 2) trunk_fwd(Args args) {
;     ...
;                 for (int e = 0; e < 8; ++e) { const int c = bb < G ? CNT[bb * 32 + e] : 0; const float tot = wave_sum((float)c), bef = wave_sum(bb < bx ? (float)c : 0.f);
;                     if (lane == 0) { atomicAdd((int*)&SH[e], (int)tot); atomicAdd((int*)&SH[8 + e], (int)bef); } } }
.LBB0_870:
	s_or_b64 exec, exec, s[12:13]
	v_mov_b32_e32 v11, 0
	s_and_saveexec_b64 s[8:9], s[6:7]
	s_cbranch_execz .LBB0_872
	v_readlane_b32 s12, v252, 18
	v_readlane_b32 s13, v252, 19
	s_waitcnt lgkmcnt(0)
	s_nop 0
	v_lshl_add_u64 v[12:13], v[4:5], 2, s[12:13]
	v_cvt_f32_i32_e32 v11, v235

; __global__ void __launch_bounds__(NWAVES * 64, 2) trunk_fwd(Args args) {
;     ...
;                 for (int e = 0; e < 8; ++e) { const int c = bb < G ? CNT[bb * 32 + e] : 0; const float tot = wave_sum((float)c), bef = wave_sum(bb < bx ? (float)c : 0.f);
;                     if (lane == 0) { atomicAdd((int*)&SH[e], (int)tot); atomicAdd((int*)&SH[8 + e], (int)bef); } } }
.LBB0_881:
	s_or_b64 exec, exec, s[12:13]
	v_mov_b32_e32 v11, 0
	s_and_saveexec_b64 s[8:9], s[6:7]
	s_cbranch_execz .LBB0_883
	v_readlane_b32 s12, v252, 18
	v_readlane_b32 s13, v252, 19
	s_waitcnt lgkmcnt(0)
	s_nop 0
	v_lshl_add_u64 v[12:13], v[4:5], 2, s[12:13]
	v_cvt_f32_i32_e32 v11, v236

; __global__ void __launch_bounds__(NWAVES * 64, 2) trunk_fwd(Args args) {
;     ...
;                 for (int e = 0; e < 8; ++e) { const int c = bb < G ? CNT[bb * 32 + e] : 0; const float tot = wave_sum((float)c), bef = wave_sum(bb < bx ? (float)c : 0.f);
;                     if (lane == 0) { atomicAdd((int*)&SH[e], (int)tot); atomicAdd((int*)&SH[8 + e], (int)bef); } } }
.LBB0_892:
	s_or_b64 exec, exec, s[12:13]
	v_mov_b32_e32 v11, 0
	s_and_saveexec_b64 s[8:9], s[6:7]
	s_cbranch_execz .LBB0_894
	v_readlane_b32 s12, v252, 18
	v_readlane_b32 s13, v252, 19
	s_waitcnt lgkmcnt(0)
	s_nop 0
	v_lshl_add_u64 v[12:13], v[4:5], 2, s[12:13]
	v_cvt_f32_i32_e32 v11, v237

; __global__ void __launch_bounds__(NWAVES * 64, 2) trunk_fwd(Args args) {
;     ...
;                 for (int e = 0; e < 8; ++e) { const int c = bb < G ? CNT[bb * 32 + e] : 0; const float tot = wave_sum((float)c), bef = wave_sum(bb < bx ? (float)c : 0.f);
;                     if (lane == 0) { atomicAdd((int*)&SH[e], (int)tot); atomicAdd((int*)&SH[8 + e], (int)bef); } } }
.LBB0_903:
	s_or_b64 exec, exec, s[12:13]
	v_mov_b32_e32 v11, 0
	s_and_saveexec_b64 s[8:9], s[6:7]
	s_cbranch_execz .LBB0_905
	v_readlane_b32 s12, v252, 18
	v_readlane_b32 s13, v252, 19
	s_waitcnt lgkmcnt(0)
	s_nop 0
	v_lshl_add_u64 v[12:13], v[4:5], 2, s[12:13]
	v_cvt_f32_i32_e32 v11, v238

; __global__ void __launch_bounds__(NWAVES * 64, 2) trunk_fwd(Args args) {
;     ...
;                 for (int e = 0; e < 8; ++e) { const int c = bb < G ? CNT[bb * 32 + e] : 0; const float tot = wave_sum((float)c), bef = wave_sum(bb < bx ? (float)c : 0.f);
;                     if (lane == 0) { atomicAdd((int*)&SH[e], (int)tot); atomicAdd((int*)&SH[8 + e], (int)bef); } } }
.LBB0_914:
	s_or_b64 exec, exec, s[12:13]
	v_mov_b32_e32 v11, 0
	s_and_saveexec_b64 s[8:9], s[6:7]
	s_cbranch_execz .LBB0_916
	v_readlane_b32 s6, v252, 18
	v_readlane_b32 s7, v252, 19
	s_nop 1
	v_cvt_f32_i32_e32 v11, v239
